# early-3-tiles prologue + ring + static prio for waves 4-7 + exact vmcnt on the last three tiles instead of vmcnt(0)
# baseline (speedup 1.0000x reference)
.Lring_tile_2:
	s_cmp_lt_u32 s30, 22
	s_cbranch_scc1 .Lring_w27_2
	s_waitcnt vmcnt(18)
	s_branch .Lring_go_2

.Lring_tile_3:
	s_cmp_lt_u32 s30, 22
	s_cbranch_scc1 .Lring_w27_3
	s_waitcnt vmcnt(9)
	s_branch .Lring_go_3
